# HGRN chunk loop waves 0/1: all K/Q fragment LDS reads issued up front with counted lgkmcnt, state fragments prefetched into the freed registers before the mask section
# speedup vs baseline: 1.0540x; 1.0025x over previous
.LBB0_302:
	v_lshlrev_b32_e32 v139, 2, v101
	v_add_u32_e32 v6, s26, v139
	v_lshl_add_u32 v2, v6, 2, 0
	v_add_u32_e32 v7, 0x10400, v2
	s_waitcnt lgkmcnt(0)
	s_barrier
	ds_read_b128 v[2:5], v7
	v_lshlrev_b32_e32 v8, 4, v100
	v_and_b32_e32 v9, 0xf0, v8
	v_lshl_add_u32 v10, v100, 8, s27
	v_lshlrev_b32_e32 v6, 1, v6
	s_waitcnt lgkmcnt(0)
	v_mul_f32_e32 v2, v84, v2
	v_mul_f32_e32 v3, v85, v3
	v_cvt_pk_bf16_f32 v2, v2, v3
	v_mul_f32_e32 v3, v86, v4
	v_mul_f32_e32 v4, v87, v5
	v_cvt_pk_bf16_f32 v3, v3, v4
	v_xad_u32 v4, v6, v9, v10
	ds_write_b64 v4, v[2:3] offset:32768
	ds_read_b128 v[2:5], v7 offset:32
	s_waitcnt lgkmcnt(0)
	v_mul_f32_e32 v2, v88, v2
	v_mul_f32_e32 v3, v89, v3
	v_cvt_pk_bf16_f32 v2, v2, v3
	v_mul_f32_e32 v3, v90, v4
	v_mul_f32_e32 v4, v91, v5
	v_cvt_pk_bf16_f32 v3, v3, v4
	v_add_u32_e32 v4, 16, v6
	v_xad_u32 v4, v4, v9, v10
	ds_write_b64 v4, v[2:3] offset:32768
	ds_read_b128 v[2:5], v7 offset:64
	s_waitcnt lgkmcnt(0)
	v_mul_f32_e32 v2, v92, v2
	v_mul_f32_e32 v3, v93, v3
	v_cvt_pk_bf16_f32 v2, v2, v3
	v_mul_f32_e32 v3, v94, v4
	v_mul_f32_e32 v4, v95, v5
	v_cvt_pk_bf16_f32 v3, v3, v4
	v_add_u32_e32 v4, 32, v6
	v_xad_u32 v4, v4, v9, v10
	ds_write_b64 v4, v[2:3] offset:32768
	ds_read_b128 v[2:5], v7 offset:96
	s_waitcnt lgkmcnt(0)
	v_mul_f32_e32 v2, v96, v2
	v_mul_f32_e32 v3, v97, v3
	v_cvt_pk_bf16_f32 v2, v2, v3
	v_mul_f32_e32 v3, v98, v4
	v_mul_f32_e32 v4, v99, v5
	v_cvt_pk_bf16_f32 v3, v3, v4
	v_add_u32_e32 v4, 48, v6
	v_xad_u32 v4, v4, v9, v10
	ds_write_b64 v4, v[2:3] offset:32768
	v_lshlrev_b32_e32 v2, 3, v100
	v_and_b32_e32 v4, 0xc0, v8
	v_lshl_add_u32 v3, v101, 8, v2
	v_and_or_b32 v2, v2, 24, v4
	v_lshlrev_b32_e32 v4, 1, v100
	v_and_b32_e32 v4, 32, v4
	v_and_b32_e32 v3, 0x100, v3
	v_or3_b32 v2, v2, v4, v3
	s_waitcnt lgkmcnt(0)
	s_barrier
	v_add_u32_e32 v3, s28, v2
	ds_read_b64_tr_b16 v[70:71], v3 offset:0
	ds_read_b64_tr_b16 v[72:73], v3 offset:0x800
	ds_read_b64_tr_b16 v[66:67], v3 offset:0x1000
	ds_read_b64_tr_b16 v[68:69], v3 offset:0x1800
	v_add_u32_e32 v6, s29, v2
	ds_read_b64_tr_b16 v[2:3], v6 offset:0
	ds_read_b64_tr_b16 v[4:5], v6 offset:0x800
	ds_read_b64_tr_b16 v[18:19], v6 offset:0x1000
	ds_read_b64_tr_b16 v[20:21], v6 offset:0x1800
	s_waitcnt lgkmcnt(0)
	v_lshlrev_b32_e32 v6, 4, v101
	v_add_u32_e32 v22, s33, v6
	v_add_u32_e32 v23, s46, v6
	v_mfma_f32_32x32x16_bf16 v[2:17], v[2:5], v[70:73], 0
	ds_read_b128 v[34:37], v22
	ds_read_b128 v[38:41], v22 offset:32
	ds_read_b128 v[58:61], v23
	ds_read_b128 v[54:57], v23 offset:32
	ds_read_b128 v[42:45], v22 offset:64
	ds_read_b128 v[50:53], v23 offset:64
	ds_read_b128 v[46:49], v22 offset:96
	ds_read_b128 v[62:65], v23 offset:96
	s_andn2_b64 vcc, exec, s[42:43]
	v_mfma_f32_32x32x16_bf16 v[2:17], v[18:21], v[66:69], v[2:17]
	s_cbranch_vccnz .LBB0_295
	ds_read_b128 v[182:185], v105 offset:8192
	ds_read_b128 v[140:143], v105
	ds_read_b128 v[186:189], v106 offset:8192
	ds_read_b128 v[144:147], v106
	ds_read_b128 v[190:193], v107 offset:8192
	ds_read_b128 v[148:151], v107
	ds_read_b128 v[194:197], v108 offset:8192
	ds_read_b128 v[74:77], v108
	ds_read_b128 v[198:201], v109 offset:8192
	ds_read_b128 v[78:81], v109
	ds_read_b128 v[202:205], v110 offset:8192
	ds_read_b128 v[156:159], v110
	ds_read_b128 v[234:237], v111 offset:8192
	ds_read_b128 v[160:163], v111
	ds_read_b128 v[238:241], v112 offset:8192
	ds_read_b128 v[152:155], v112
	v_cmp_le_i32_e32 vcc, v139, v100
	v_or_b32_e32 v172, 2, v139
	v_or_b32_e32 v173, 3, v139
	v_add_u32_e32 v174, 8, v139
	v_add_u32_e32 v175, 9, v139
	v_add_u32_e32 v176, 10, v139
	v_add_u32_e32 v177, 11, v139
	v_add_u32_e32 v178, 24, v139
	v_add_u32_e32 v179, 25, v139
	v_add_u32_e32 v180, 26, v139
	s_lshl_b32 s56, s7, 5
	s_cmp_gt_i32 s7, 7
	s_cselect_b32 s7, s90, 0xff
	s_sub_i32 s7, s7, s56
	s_and_b64 s[76:77], s[10:11], exec
	s_cselect_b32 s7, s56, s7
	s_add_i32 s76, s7, s3
	s_ashr_i32 s77, s76, 31
	s_lshl_b64 s[76:77], s[76:77], 11
	s_add_u32 s76, s47, s76
	s_addc_u32 s77, s52, s77
	v_add_u32_e32 v164, 16, v139
	v_add_u32_e32 v165, 17, v139
	v_add_u32_e32 v166, 18, v139
	v_add_u32_e32 v167, 19, v139
	s_waitcnt lgkmcnt(14)
	v_mfma_f32_32x32x16_bf16 v[18:33], v[182:185], v[140:143], 0
	s_waitcnt lgkmcnt(12)
	v_mfma_f32_32x32x16_bf16 v[18:33], v[186:189], v[144:147], v[18:33]
	s_waitcnt lgkmcnt(10)
	v_mfma_f32_32x32x16_bf16 v[18:33], v[190:193], v[148:151], v[18:33]
	s_waitcnt lgkmcnt(8)
	v_mfma_f32_32x32x16_bf16 v[18:33], v[194:197], v[74:77], v[18:33]
	s_waitcnt lgkmcnt(6)
	v_mfma_f32_32x32x16_bf16 v[18:33], v[198:201], v[78:81], v[18:33]
	s_waitcnt lgkmcnt(4)
	v_mfma_f32_32x32x16_bf16 v[18:33], v[202:205], v[156:159], v[18:33]
	s_waitcnt lgkmcnt(2)
	v_mfma_f32_32x32x16_bf16 v[18:33], v[234:237], v[160:163], v[18:33]
	s_waitcnt lgkmcnt(0)
	v_mfma_f32_32x32x16_bf16 v[18:33], v[238:241], v[152:155], v[18:33]
	v_add_u32_e32 v242, s27, v105
	ds_read_b128 v[182:185], v242 offset:32768
	v_add_u32_e32 v242, s27, v106
	ds_read_b128 v[186:189], v242 offset:32768
	v_add_u32_e32 v242, s27, v107
	ds_read_b128 v[190:193], v242 offset:32768
	v_add_u32_e32 v242, s27, v108
	ds_read_b128 v[194:197], v242 offset:32768
	v_add_u32_e32 v242, s27, v109
	ds_read_b128 v[198:201], v242 offset:32768
	v_add_u32_e32 v242, s27, v110
	ds_read_b128 v[202:205], v242 offset:32768
	v_add_u32_e32 v242, s27, v111
	ds_read_b128 v[234:237], v242 offset:32768
	v_add_u32_e32 v242, s27, v112
	ds_read_b128 v[238:241], v242 offset:32768
	v_cndmask_b32_e32 v18, 0, v18, vcc
	v_cmp_lt_i32_e32 vcc, v139, v100
	v_add_u32_e32 v139, 27, v139
	s_nop 0
	v_cndmask_b32_e32 v19, 0, v19, vcc
	v_cmp_le_i32_e32 vcc, v172, v100
	v_cvt_pk_bf16_f32 v18, v18, v19
	s_nop 1
	v_cndmask_b32_e32 v20, 0, v20, vcc
	v_cmp_le_i32_e32 vcc, v173, v100
	s_nop 1
	v_cndmask_b32_e32 v21, 0, v21, vcc
	v_cmp_le_i32_e32 vcc, v174, v100
	v_cvt_pk_bf16_f32 v19, v20, v21
	s_nop 1
	v_cndmask_b32_e32 v22, 0, v22, vcc
	v_cmp_le_i32_e32 vcc, v175, v100
	s_nop 1
	v_cndmask_b32_e32 v23, 0, v23, vcc
	v_cmp_le_i32_e32 vcc, v176, v100
	v_cvt_pk_bf16_f32 v20, v22, v23
	s_nop 0
	v_permlane32_swap_b32_e32 v18, v20
	v_cndmask_b32_e32 v24, 0, v24, vcc
	v_cmp_le_i32_e32 vcc, v177, v100
	s_nop 1
	v_cndmask_b32_e32 v25, 0, v25, vcc
	v_cmp_le_i32_e32 vcc, v164, v100
	v_cvt_pk_bf16_f32 v21, v24, v25
	s_nop 0
	v_permlane32_swap_b32_e32 v19, v21
	v_cndmask_b32_e32 v26, 0, v26, vcc
	v_cmp_le_i32_e32 vcc, v165, v100
	s_nop 1
	v_cndmask_b32_e32 v27, 0, v27, vcc
	v_cmp_le_i32_e32 vcc, v166, v100
	v_cvt_pk_bf16_f32 v164, v26, v27
	s_nop 1
	v_cndmask_b32_e32 v28, 0, v28, vcc
	v_cmp_le_i32_e32 vcc, v167, v100
	s_nop 1
	v_cndmask_b32_e32 v29, 0, v29, vcc
	v_cmp_le_i32_e32 vcc, v178, v100
	v_cvt_pk_bf16_f32 v165, v28, v29
	s_nop 1
	v_cndmask_b32_e32 v30, 0, v30, vcc
	v_cmp_le_i32_e32 vcc, v179, v100
	s_nop 1
	v_cndmask_b32_e32 v31, 0, v31, vcc
	v_cmp_le_i32_e32 vcc, v180, v100
	v_cvt_pk_bf16_f32 v166, v30, v31
	s_nop 0
	v_permlane32_swap_b32_e32 v164, v166
	v_cndmask_b32_e32 v32, 0, v32, vcc
	v_cmp_le_i32_e32 vcc, v139, v100
	v_add_u32_e32 v139, s27, v110
	s_nop 0
	v_cndmask_b32_e32 v33, 0, v33, vcc
	v_cvt_pk_bf16_f32 v167, v32, v33
	v_mfma_f32_32x32x16_bf16 v[18:33], v[18:21], v[70:73], 0
	v_permlane32_swap_b32_e32 v165, v167
	s_nop 1
	v_mfma_f32_32x32x16_bf16 v[18:33], v[164:167], v[66:69], v[18:33]
	s_waitcnt lgkmcnt(0)
	v_mfma_f32_32x32x16_bf16 v[18:33], v[140:143], v[182:185], v[18:33]
	v_mul_lo_u32 v140, s53, v101
	v_ashrrev_i32_e32 v141, 31, v140
	v_ashrrev_i32_e32 v101, 31, v100
	v_mfma_f32_32x32x16_bf16 v[18:33], v[144:147], v[186:189], v[18:33]
	v_mfma_f32_32x32x16_bf16 v[18:33], v[148:151], v[190:193], v[18:33]
	v_mfma_f32_32x32x16_bf16 v[18:33], v[74:77], v[194:197], v[18:33]
	v_mfma_f32_32x32x16_bf16 v[18:33], v[78:81], v[198:201], v[18:33]
	v_lshl_add_u64 v[66:67], v[140:141], 2, s[76:77]
	v_lshl_add_u64 v[74:75], v[100:101], 2, v[66:67]
	v_lshl_add_u64 v[76:77], s[62:63], 2, v[74:75]
	v_lshl_add_u64 v[78:79], v[76:77], 0, s[86:87]
	v_lshl_add_u64 v[80:81], v[78:79], 0, s[86:87]
	v_lshl_add_u64 v[100:101], v[80:81], 0, s[50:51]
	v_mfma_f32_32x32x16_bf16 v[18:33], v[156:159], v[202:205], v[18:33]
	v_lshl_add_u64 v[140:141], v[100:101], 0, s[86:87]
	v_mfma_f32_32x32x16_bf16 v[18:33], v[160:163], v[234:237], v[18:33]
	v_lshl_add_u64 v[66:67], v[140:141], 0, s[86:87]
	v_lshl_add_u64 v[68:69], v[66:67], 0, s[86:87]
	v_lshl_add_u64 v[142:143], v[68:69], 0, s[50:51]
	v_lshl_add_u64 v[144:145], v[142:143], 0, s[86:87]
	v_lshl_add_u64 v[146:147], v[144:145], 0, s[86:87]
	v_lshl_add_u64 v[148:149], v[146:147], 0, s[86:87]
	v_lshl_add_u64 v[150:151], v[148:149], 0, s[50:51]
	v_mfma_f32_32x32x16_bf16 v[18:33], v[152:155], v[238:241], v[18:33]
	s_nop 11
	global_store_dword v[74:75], v18, off
	global_store_dword v[76:77], v19, off
	global_store_dword v[78:79], v20, off
	global_store_dword v[80:81], v21, off
	global_store_dword v[100:101], v22, off
	global_store_dword v[140:141], v23, off
	global_store_dword v[66:67], v24, off
	global_store_dword v[68:69], v25, off
	global_store_dword v[142:143], v26, off
	global_store_dword v[144:145], v27, off
	global_store_dword v[146:147], v28, off
	global_store_dword v[148:149], v29, off
	global_store_dword v[150:151], v30, off
	v_lshl_add_u64 v[18:19], v[150:151], 0, s[86:87]
	global_store_dword v[18:19], v31, off
	v_lshl_add_u64 v[18:19], v[18:19], 0, s[86:87]
	global_store_dword v[18:19], v32, off
	v_lshl_add_u64 v[18:19], v[18:19], 0, s[86:87]
	global_store_dword v[18:19], v33, off
	s_branch .LBB0_295
